# v40: v34 + one static s_setprio 1 for waves 4-7 during the attention loop (timing only), reset at the end of the phase
# speedup vs baseline: 1.0044x; 1.0044x over previous
; __device__ __forceinline__ int v_st(int k, int c) { const int kk = (k & ~0xC) | ((k & 4) << 1) | ((k & 8) >> 1); return ((kk >> 3) * 4 + (c >> 5)) * 512 + ((kk & 7) * 32 + (c & 31)) * 2; }
; __device__ __forceinline__ int v_rd_base(int lane) { return ((lane & 3) << 3) | (((lane >> 2) & 3) << 6) | (((lane >> 4) & 1) << 5) | (((lane >> 5) & 1) << 8); }
; #define FOX_RANGE(ii, ja_, jb_, h_, qb_, p_) do { h_ = (ii) >> 5; qb_ = (ii) & 31; const int ex_ = prefL[ii]; ja_ = jloL[ii] + (start > ex_ ? start - ex_ : 0); \
;         jb_ = jloL[ii] + ((end - ex_ < costL[ii]) ? end - ex_ : costL[ii]); p_ = F.vcu - ownL[ii]; } while (0)
; template <class TIn, class TOut>
; __device__ __forceinline__ void causal_swa_block(const BlockRef<TIn, TOut>& cur, const BlockRef<TIn, TOut>& nxt, int skv, int W, char* lds, Seam<TIn>& S) {
;     ...
;     const int qlo = cur.P0 + wid * QBLK, qm = qlo + r32 - 4 * hi;
;     char* V_lds = lds; char* K_lds = lds + 2 * SHM_V;
;     float* ws = (float*)(lds + 2 * SHM_V + 2 * SHM_K) + wid * 64; float* li_l = ws, * al_l = ws + 32;
;     const float* biasL = (const float*)(lds + ATT_BIAS_OFF);
;     float m_reg = -1e30f, l_reg = 0; f32x16 o[4] = {};
;     const int sr = tid >> 4, sc = (tid & 15) * 8, vst0 = v_st(sr, sc), vst1 = v_st(32 + sr, sc), kws = KSWZ(sr, sc * 2);
;     const int vb0 = (int)(uintptr_t)V_lds + v_rd_base(lane);
; __device__ __forceinline__ void ph5_attention(const Frame& F, const Args& A, char* lds) {
;     ...
;     int i = 0; { int lo = 0, hi = 255; while (lo < hi) { const int mid = (lo + hi + 1) >> 1; if (prefL[mid] <= start) lo = mid; else hi = mid - 1; } i = lo; }
;     ...
;     int h, qb, ja, jb, p; FOX_RANGE(i, ja, jb, h, qb, p);
;     fox::BlockRef<fbf, fbf> cur = FOX_REF(h, qb, ja, jb, p);
;     fox::Seam<fbf> S;
;     int cur_h = -1;
.LBB0_691:
	s_add_i32 s2, s0, s1
	s_add_i32 s2, s2, 1
	s_ashr_i32 s2, s2, 1
	s_lshl_b32 s3, s2, 2
	s_add_i32 s3, s3, 0
	s_add_i32 s3, s3, 0x1a800
	v_mov_b32_e32 v2, s3
	ds_read_b32 v2, v2
	s_add_i32 s3, s2, -1
	s_waitcnt lgkmcnt(0)
	v_readfirstlane_b32 s4, v2
	s_cmp_gt_i32 s4, s16
	s_cselect_b32 s1, s3, s1
	s_cselect_b32 s0, s0, s2
	s_cmp_lt_i32 s0, s1
	s_cbranch_scc1 .LBB0_691
	s_add_u32 s19, s88, 0x6e00000
	s_addc_u32 s40, s89, 0
	s_add_u32 s41, s88, 0x7e00000
	s_addc_u32 s42, s89, 0
	s_add_u32 s43, s88, 0x17e02800
	s_addc_u32 s44, s89, 0
	s_add_u32 s45, s88, 0x70e00000
	s_addc_u32 s46, s89, 0
	s_add_u32 s47, s88, 0x90e00000
	s_addc_u32 s48, s89, 0
	s_lshl_b32 s2, s0, 2
	s_add_i32 s6, s2, 0
	s_add_i32 s2, s6, 0x1a800
	v_mov_b32_e32 v2, s2
	ds_read_b32 v2, v2
	s_add_i32 s2, s6, 0x1ac20
	v_mov_b32_e32 v3, s2
	ds_read_b32 v3, v3
	s_ashr_i32 s10, s0, 5
	s_waitcnt lgkmcnt(1)
	v_readfirstlane_b32 s2, v2
	s_and_b32 s49, s0, 31
	s_ashr_i32 s1, s0, 31
	s_sub_i32 s3, s16, s2
	s_cmp_gt_i32 s16, s2
	s_cselect_b32 s3, s3, 0
	s_waitcnt lgkmcnt(0)
	v_readfirstlane_b32 s4, v3
	s_add_i32 s68, s3, s4
	s_add_i32 s3, s6, 0x1a400
	v_mov_b32_e32 v2, s3
	ds_read_b32 v2, v2
	s_add_i32 s3, s6, 0x1d400
	v_mov_b32_e32 v3, s3
	ds_read_b32 v3, v3
	s_sub_i32 s2, s17, s2
	s_waitcnt lgkmcnt(1)
	v_readfirstlane_b32 s3, v2
	s_min_i32 s2, s2, s3
	s_add_i32 s66, s2, s4
	s_waitcnt lgkmcnt(0)
	v_readfirstlane_b32 s2, v3
	v_readlane_b32 s3, v254, 4
	s_sub_i32 s50, s3, s2
	s_lshl_b32 s2, s49, 19
	s_add_u32 s4, s19, s2
	s_addc_u32 s5, s40, 0
	s_lshl_b32 s2, s10, 7
	s_ashr_i32 s3, s2, 31
	s_lshl_b64 s[2:3], s[2:3], 1
	s_add_u32 s12, s4, s2
	s_addc_u32 s13, s5, s3
	s_add_u32 s8, s41, s2
	s_addc_u32 s9, s42, s3
	s_add_u32 s36, s43, s2
	s_addc_u32 s37, s44, s3
	s_lshl_b32 s33, s49, 8
	s_lshl_b64 s[2:3], s[0:1], 4
	s_ashr_i32 s1, s50, 31
	s_add_u32 s2, s2, s50
	v_lshrrev_b32_e32 v195, 4, v0
	v_lshrrev_b32_e32 v11, 3, v0
	s_addc_u32 s3, s3, s1
	v_or_b32_e32 v199, 32, v195
	v_and_b32_e32 v11, 8, v11
	s_lshl_b64 s[4:5], s[2:3], 16
	v_lshlrev_b32_e32 v4, 3, v0
	v_and_or_b32 v12, v195, 16, v11
	v_and_or_b32 v11, v199, 48, v11
	s_add_u32 s34, s45, s4
	v_and_b32_e32 v198, 0x78, v4
	v_lshrrev_b32_e32 v13, 5, v0
	v_lshrrev_b32_e32 v12, 1, v12
	v_bfe_u32 v14, v4, 5, 2
	v_bfe_u32 v15, v0, 4, 2
	v_lshrrev_b32_e32 v11, 1, v11
	s_addc_u32 s35, s46, s5
	s_lshl_b64 s[2:3], s[2:3], 11
	v_lshlrev_b32_e32 v5, 1, v198
	v_or_b32_e32 v12, v12, v14
	v_and_or_b32 v13, v13, 4, v15
	v_or_b32_e32 v11, v11, v14
	s_add_u32 s20, s47, s2
	v_lshlrev_b32_e32 v3, 8, v195
	s_movk_i32 s1, 0x70
	v_and_b32_e32 v6, 0x70, v0
	v_lshlrev_b32_e32 v12, 9, v12
	v_lshlrev_b32_e32 v13, 6, v13
	v_and_b32_e32 v15, 48, v5
	v_lshlrev_b32_e32 v11, 9, v11
	s_addc_u32 s21, s48, s3
	v_bitop3_b32 v7, v5, v0, s1 bitop3:0x78
	v_add_u32_e32 v8, 0, v3
	v_or3_b32 v12, v12, v13, v15
	v_or3_b32 v11, v11, v13, v15
	v_bitop3_b32 v3, v5, v3, v6 bitop3:0xde
	v_lshlrev_b32_e32 v5, 4, v0
	v_lshlrev_b32_e32 v13, 1, v0
	v_bfe_u32 v10, v0, 5, 1
	v_and_b32_e32 v6, 0xc0, v5
	v_and_b32_e32 v13, 32, v13
	v_and_b32_e32 v4, 0x118, v4
	s_cmp_lg_u32 0, -1
	v_or3_b32 v4, v13, v6, v4
	s_cselect_b32 s1, 0, 0
	v_lshlrev_b32_e32 v6, 4, v10
	v_and_b32_e32 v194, 31, v0
	v_lshrrev_b32_e32 v2, 2, v0
	v_and_b32_e32 v9, 63, v0
	v_lshlrev_b32_e32 v210, 2, v10
	v_add_u32_e32 v212, s1, v4
	s_add_i32 s1, 0, 0x11000
	v_and_b32_e32 v4, 0x70, v5
	v_or_b32_e32 v14, 32, v6
	v_or_b32_e32 v15, 64, v6
	v_or_b32_e32 v16, 0x60, v6
	v_and_b32_e32 v2, 8, v2
	v_mov_b32_e32 v197, 0
	v_sub_u32_e32 v211, v194, v210
	v_add_u32_e32 v213, s1, v6
	v_lshlrev_b32_e32 v13, 8, v194
	v_xad_u32 v5, v6, v4, 0
	v_xad_u32 v14, v14, v4, 0
	v_xad_u32 v15, v15, v4, 0
	v_xad_u32 v16, v16, v4, 0
	v_cmp_gt_u32_e64 s[2:3], 32, v9
	v_lshlrev_b32_e32 v4, 3, v10
	v_and_b32_e32 v9, 1, v0
	s_add_u32 s14, s88, 0xe00000
	v_add_u32_e32 v6, 0, v6
	s_mov_b32 s11, 0
	s_mov_b32 s61, -1
	v_cmp_eq_u32_e64 s[4:5], 0, v9
	v_lshlrev_b32_e32 v200, 10, v10
	v_mov_b32_e32 v201, v197
	s_addc_u32 s15, s89, 0
	s_add_i32 s51, s6, 0x1a404
	v_add_u32_e32 v214, 0xffffdf45, v211
	v_add_u32_e32 v215, 0x11100, v6
	v_lshlrev_b32_e32 v202, 1, v2
	s_movk_i32 s52, 0x5800
	v_add_u32_e32 v216, v8, v7
	s_movk_i32 s53, 0x2000
	s_movk_i32 s54, 0xdfff
	s_mov_b32 s55, 0x41000000
	s_mov_b32 s18, 0x3e0293ee
	v_lshlrev_b32_e32 v204, 1, v4
	v_add_u32_e32 v217, 0, v12
	v_add_u32_e32 v218, 0, v11
	v_add_u32_e32 v219, v5, v13
	v_add_u32_e32 v220, v14, v13
	v_add_u32_e32 v221, v15, v13
	v_add_u32_e32 v222, v16, v13
	v_mov_b32_e32 v223, 0xff800000
	v_add_u32_e32 v224, 0, v3
	v_mov_b32_e32 v225, 0xf149f2ca
	s_mov_b32 s58, s68
	s_mov_b32 s59, s66
	v_readlane_b32 s98, v254, 32
	s_cmp_ge_u32 s98, 4
	s_cbranch_scc0 .Lattn_prio_done
	s_setprio 1
.Lattn_prio_done:
	s_branch .LBB0_695
.LBB0_693:
	s_add_i32 s51, s51, 4
	s_mov_b64 s[0:1], 0
	s_mov_b64 s[20:21], s[30:31]
	s_mov_b64 s[8:9], s[22:23]
	s_mov_b64 s[36:37], s[24:25]
	s_mov_b32 s33, s63
	s_mov_b32 s68, s65
	s_mov_b32 s66, s64
	s_mov_b64 s[34:35], s[26:27]

; __device__ __forceinline__ unsigned xb_ld(unsigned* p)              { return __hip_atomic_load(p, __ATOMIC_RELAXED, __HIP_MEMORY_SCOPE_AGENT); }
; __device__ __forceinline__ unsigned xb_add(unsigned* p, unsigned v) { return __hip_atomic_fetch_add(p, v, __ATOMIC_RELAXED, __HIP_MEMORY_SCOPE_AGENT); }
; #define XB_SPIN(cond, bar) do { unsigned _sp = 0; while (cond) { __builtin_amdgcn_s_sleep(1); \
;     if ((++_sp & 255u) == 0u) { if (xb_ld(&(bar)[XB_TMO])) break; if (_sp > XB_SPIN_CAP) { atomicAdd(&(bar)[XB_TMO], 1u); break; } } } } while (0)
; __device__ __forceinline__ void xcd_barrier(const XcdBarrier& b) {
;     asm volatile("s_waitcnt vmcnt(0)" ::: "memory");
;     __syncthreads();
;     if (threadIdx.x == 0) {
;         unsigned* bar = b.bar;
;         __builtin_amdgcn_s_waitcnt(0);
;         unsigned nloc = b.st[0], nx = b.st[1];
;         if (nloc == 0u) { xcd_barrier_complete(bar, b.x, nloc, nx); b.st[0] = nloc; b.st[1] = nx; }
;         const unsigned old = xb_add(&bar[XB_XSUB(b.x)], 1u);
;         const unsigned gen = old / nloc;
;         if (old + 1u == (gen + 1u) * nloc) {
;             __builtin_amdgcn_fence(__ATOMIC_RELEASE, "agent");
;             asm volatile("s_waitcnt vmcnt(0)" ::: "memory");
;             const unsigned og = xb_add(&bar[XB_TOP], 1u);
;             const unsigned tg = og / nx;
;             if (og + 1u == (tg + 1u) * nx) xb_add(&bar[XB_TOPGEN], 1u);
;             else XB_SPIN(xb_ld(&bar[XB_TOPGEN]) == tg, bar);
;             __builtin_amdgcn_fence(__ATOMIC_ACQUIRE, "agent");
;             xb_add(&bar[XB_XGEN(b.x)], 1u);
;             asm volatile("s_waitcnt vmcnt(0)" ::: "memory");
.LBB0_882:
	s_setprio 0
	v_readlane_b32 s0, v254, 9
	v_readlane_b32 s1, v254, 10
	s_cmp_gt_i32 s1, 6
	s_cselect_b64 s[0:1], -1, 0
	s_and_b64 s[2:3], s[80:81], s[0:1]
	s_andn2_b64 vcc, exec, s[2:3]
	s_cbranch_vccnz .LBB0_938
	s_waitcnt vmcnt(0)
	s_waitcnt vmcnt(0)
	s_barrier
	s_mov_b64 s[2:3], exec
	v_readlane_b32 s4, v254, 14
	v_readlane_b32 s5, v254, 15
	s_and_b64 s[4:5], s[2:3], s[4:5]
	s_mov_b64 exec, s[4:5]
	s_cbranch_execz .LBB0_937
	s_add_i32 s4, 0, 0x20020
	v_mov_b32_e32 v1, s4
	s_waitcnt vmcnt(0) expcnt(0) lgkmcnt(0)
	ds_read_b32 v3, v1
	s_add_i32 s4, 0, 0x20024
	v_mov_b32_e32 v1, s4
	ds_read_b32 v1, v1
	s_waitcnt lgkmcnt(1)
	v_cmp_ne_u32_e32 vcc, 0, v3
	s_cbranch_vccnz .LBB0_901
	v_readlane_b32 s4, v254, 1
	v_readlane_b32 s5, v254, 2
	s_load_dwordx2 s[8:9], s[4:5], 0x4
	s_add_u32 s4, s88, 0x4200
	s_addc_u32 s5, s89, 0
	s_add_u32 s6, s88, 0x4400
	s_addc_u32 s7, s89, 0
	s_waitcnt lgkmcnt(0)
	s_mul_i32 s33, s8, s92
	s_add_u32 s8, s88, 0x4500
	s_mul_i32 s33, s33, s9
	s_addc_u32 s9, s89, 0
	s_add_u32 s10, s88, 0x4600
	s_addc_u32 s11, s89, 0
	s_add_u32 s12, s88, 0x4700
	s_addc_u32 s13, s89, 0
	s_add_u32 s14, s88, 0x4800
	s_addc_u32 s15, s89, 0
	s_add_u32 s16, s88, 0x4900
	s_addc_u32 s17, s89, 0
	s_add_u32 s18, s88, 0x4a00
	s_addc_u32 s19, s89, 0
	s_add_u32 s20, s88, 0x4b00
	s_addc_u32 s21, s89, 0
	s_add_u32 s22, s88, 0x4c00
	s_addc_u32 s23, s89, 0
	s_add_u32 s24, s88, 0x4d00
	s_addc_u32 s25, s89, 0
	s_add_u32 s26, s88, 0x4e00
	s_addc_u32 s27, s89, 0
	s_add_u32 s28, s88, 0x4f00
	s_addc_u32 s29, s89, 0
	s_add_u32 s30, s88, 0x5000
	s_addc_u32 s31, s89, 0
	s_add_u32 s34, s88, 0x5100
	s_addc_u32 s35, s89, 0
	s_add_u32 s36, s88, 0x5200
	s_addc_u32 s37, s89, 0
	s_add_u32 s38, s88, 0x5300
	s_addc_u32 s39, s89, 0
	s_mov_b32 s46, 1
	v_mov_b32_e32 v17, 0
	s_branch .LBB0_887
